# attention select, rows shorter than 1024: the 12 masked score loads issued together with one wait (was a load+wait per value)
# speedup vs baseline: 1.0002x; 1.0002x over previous
.LBB0_895:
	s_and_b64 vcc, exec, s[14:15]
	s_cbranch_vccz .LBB0_921
	global_load_ushort v17, v146, s[78:79]
	global_load_ushort v19, v146, s[78:79] offset:128
	global_load_ushort v20, v146, s[78:79] offset:256
	global_load_ushort v21, v146, s[78:79] offset:384
	v_mov_b32_e32 v147, v3
	v_lshl_add_u64 v[4:5], s[78:79], 0, v[146:147]
	v_cmp_ge_u32_e32 vcc, s76, v156
	v_mov_b32_e32 v14, 0xff800000
	v_mov_b32_e32 v16, 0xff800000
	s_and_saveexec_b64 s[12:13], vcc
	s_cbranch_execz .LBB0_898
	global_load_ushort v238, v[4:5], off offset:512
.LBB0_898:
	s_or_b64 exec, exec, s[12:13]
	v_cmp_ge_u32_e32 vcc, s76, v157
	s_and_saveexec_b64 s[12:13], vcc
	s_cbranch_execz .LBB0_900
	global_load_ushort v239, v[4:5], off offset:640
.LBB0_900:
	s_or_b64 exec, exec, s[12:13]
	v_cmp_ge_u32_e32 vcc, s76, v158
	v_mov_b32_e32 v12, 0xff800000
	v_mov_b32_e32 v15, 0xff800000
	s_and_saveexec_b64 s[12:13], vcc
	s_cbranch_execz .LBB0_902
	global_load_ushort v240, v[4:5], off offset:768
.LBB0_902:
	s_or_b64 exec, exec, s[12:13]
	v_cmp_ge_u32_e32 vcc, s76, v159
	s_and_saveexec_b64 s[12:13], vcc
	s_cbranch_execz .LBB0_904
	global_load_ushort v241, v[4:5], off offset:896
.LBB0_904:
	s_or_b64 exec, exec, s[12:13]
	v_cmp_ge_u32_e32 vcc, s76, v160
	v_mov_b32_e32 v10, 0xff800000
	v_mov_b32_e32 v13, 0xff800000
	s_and_saveexec_b64 s[12:13], vcc
	s_cbranch_execz .LBB0_906
	global_load_ushort v242, v[4:5], off offset:1024
.LBB0_906:
	s_or_b64 exec, exec, s[12:13]
	v_cmp_ge_u32_e32 vcc, s76, v161
	s_and_saveexec_b64 s[12:13], vcc
	s_cbranch_execz .LBB0_908
	global_load_ushort v243, v[4:5], off offset:1152
.LBB0_908:
	s_or_b64 exec, exec, s[12:13]
	v_cmp_ge_u32_e32 vcc, s76, v162
	v_mov_b32_e32 v8, 0xff800000
	v_mov_b32_e32 v11, 0xff800000
	s_and_saveexec_b64 s[12:13], vcc
	s_cbranch_execz .LBB0_910
	global_load_ushort v244, v[4:5], off offset:1280
.LBB0_910:
	s_or_b64 exec, exec, s[12:13]
	v_cmp_ge_u32_e32 vcc, s76, v163
	s_and_saveexec_b64 s[12:13], vcc
	s_cbranch_execz .LBB0_912
	global_load_ushort v245, v[4:5], off offset:1408
.LBB0_912:
	s_or_b64 exec, exec, s[12:13]
	v_cmp_ge_u32_e32 vcc, s76, v164
	v_mov_b32_e32 v6, 0xff800000
	v_mov_b32_e32 v9, 0xff800000
	s_and_saveexec_b64 s[12:13], vcc
	s_cbranch_execz .LBB0_914
	global_load_ushort v246, v[4:5], off offset:1536
.LBB0_914:
	s_or_b64 exec, exec, s[12:13]
	v_cmp_ge_u32_e32 vcc, s76, v165
	s_and_saveexec_b64 s[12:13], vcc
	s_cbranch_execz .LBB0_916
	global_load_ushort v247, v[4:5], off offset:1664
.LBB0_916:
	s_or_b64 exec, exec, s[12:13]
	v_cmp_ge_u32_e32 vcc, s76, v166
	v_mov_b32_e32 v2, 0xff800000
	v_mov_b32_e32 v7, 0xff800000
	s_and_saveexec_b64 s[12:13], vcc
	s_cbranch_execz .LBB0_918
	global_load_ushort v248, v[4:5], off offset:1792
.LBB0_918:
	s_or_b64 exec, exec, s[12:13]
	v_cmp_ge_u32_e32 vcc, s76, v138
	s_and_saveexec_b64 s[12:13], vcc
	s_cbranch_execz .LBB0_920
	global_load_ushort v249, v184, s[78:79]
.LBB0_920:
	s_or_b64 exec, exec, s[12:13]
	s_waitcnt vmcnt(0)
	v_cvt_f32_f16_e32 v250, v238
	v_cmp_ge_u32_e32 vcc, s76, v156
	v_cndmask_b32_e32 v16, v16, v250, vcc
	v_cvt_f32_f16_e32 v250, v239
	v_cmp_ge_u32_e32 vcc, s76, v157
	v_cndmask_b32_e32 v14, v14, v250, vcc
	v_cvt_f32_f16_e32 v250, v240
	v_cmp_ge_u32_e32 vcc, s76, v158
	v_cndmask_b32_e32 v15, v15, v250, vcc
	v_cvt_f32_f16_e32 v250, v241
	v_cmp_ge_u32_e32 vcc, s76, v159
	v_cndmask_b32_e32 v12, v12, v250, vcc
	v_cvt_f32_f16_e32 v250, v242
	v_cmp_ge_u32_e32 vcc, s76, v160
	v_cndmask_b32_e32 v13, v13, v250, vcc
	v_cvt_f32_f16_e32 v250, v243
	v_cmp_ge_u32_e32 vcc, s76, v161
	v_cndmask_b32_e32 v10, v10, v250, vcc
	v_cvt_f32_f16_e32 v250, v244
	v_cmp_ge_u32_e32 vcc, s76, v162
	v_cndmask_b32_e32 v11, v11, v250, vcc
	v_cvt_f32_f16_e32 v250, v245
	v_cmp_ge_u32_e32 vcc, s76, v163
	v_cndmask_b32_e32 v8, v8, v250, vcc
	v_cvt_f32_f16_e32 v250, v246
	v_cmp_ge_u32_e32 vcc, s76, v164
	v_cndmask_b32_e32 v9, v9, v250, vcc
	v_cvt_f32_f16_e32 v250, v247
	v_cmp_ge_u32_e32 vcc, s76, v165
	v_cndmask_b32_e32 v6, v6, v250, vcc
	v_cvt_f32_f16_e32 v250, v248
	v_cmp_ge_u32_e32 vcc, s76, v166
	v_cndmask_b32_e32 v7, v7, v250, vcc
	v_cvt_f32_f16_e32 v250, v249
	v_cmp_ge_u32_e32 vcc, s76, v138
	v_cndmask_b32_e32 v2, v2, v250, vcc
	s_waitcnt vmcnt(3)
	v_cvt_f32_f16_e32 v18, v17
	s_waitcnt vmcnt(2)
	v_cvt_f32_f16_e32 v17, v19
	s_waitcnt vmcnt(1)
	v_cvt_f32_f16_e32 v5, v20
	s_waitcnt vmcnt(0)
	v_cvt_f32_f16_e32 v4, v21
	s_mov_b32 s16, -1
